# speedup vs baseline: 1.0884x; 1.0067x over previous
.LBB2_56:
	v_add_u32_e32 v228, 0, v110
	v_lshrrev_b32_e32 v229, 3, v228
	v_and_b32_e32 v228, 7, v228
	v_lshlrev_b32_e32 v228, 4, v228
	v_lshl_or_b32 v228, v229, 8, v228
	global_load_dwordx4 v[208:211], v228, s[58:59]
	v_add_u32_e32 v228, 64, v110
	v_lshrrev_b32_e32 v229, 3, v228
	v_and_b32_e32 v228, 7, v228
	v_lshlrev_b32_e32 v228, 4, v228
	v_lshl_or_b32 v228, v229, 8, v228
	global_load_dwordx4 v[212:215], v228, s[58:59]
	v_add_u32_e32 v228, 128, v110
	v_lshrrev_b32_e32 v229, 3, v228
	v_and_b32_e32 v228, 7, v228
	v_lshlrev_b32_e32 v228, 4, v228
	v_lshl_or_b32 v228, v229, 8, v228
	global_load_dwordx4 v[216:219], v228, s[58:59]
	v_add_u32_e32 v228, 192, v110
	v_lshrrev_b32_e32 v229, 3, v228
	v_and_b32_e32 v228, 7, v228
	v_lshlrev_b32_e32 v228, 4, v228
	v_lshl_or_b32 v228, v229, 8, v228
	global_load_dwordx4 v[220:223], v228, s[58:59]
	v_add_u32_e32 v228, 256, v110
	v_lshrrev_b32_e32 v229, 3, v228
	v_and_b32_e32 v228, 7, v228
	v_lshlrev_b32_e32 v228, 4, v228
	v_lshl_or_b32 v228, v229, 8, v228
	global_load_dwordx4 v[224:227], v228, s[58:59]
	v_lshlrev_b32_e32 v228, 4, v110
	v_add_u32_e32 v228, 0x26000, v228
	s_waitcnt vmcnt(0)
	ds_write_b128 v228, v[208:211]
	ds_write_b128 v228, v[212:215] offset:1024
	ds_write_b128 v228, v[216:219] offset:2048
	ds_write_b128 v228, v[220:223] offset:3072
	ds_write_b128 v228, v[224:227] offset:4096
	v_cvt_f32_f16_e32 v184, v1
	v_mov_b32_e32 v185, 0xff61b1e6
	v_mov_b32_e32 v195, 0xff61b1e6
	s_waitcnt lgkmcnt(0)
	s_barrier

.Lmk_p72:
	s_cmp_ge_u32 s38, 4
	s_cbranch_scc0 .Lmk_prio_done
	s_setprio 1
.Lmk_prio_done:
	v_mov_b64_e32 v[168:169], s[12:13]
	v_mov_b64_e32 v[170:171], s[12:13]
	v_xor_b32_e32 v117, 64, v122
	s_mov_b32 s30, s85
	s_lshl_b32 s6, s43, 6
	s_sub_i32 s83, s44, s6
	s_lshl_b32 s6, s43, 8
	s_add_i32 s82, s78, s6
	s_mov_b32 s66, s41
	s_branch .LBB2_62

.LBB2_64:
	v_bfe_u32 v34, v121, 16, 4
	v_cmp_gt_i32_e64 s[56:57], s66, v110
	v_lshl_add_u32 v115, v34, 1, v191
	v_lshlrev_b32_e32 v34, 2, v34
	ds_bpermute_b32 v121, v34, v197
	ds_read_b128 v[208:211], v122
	ds_read_b128 v[212:215], v117
	ds_read_b128 v[216:219], v122 offset:2048
	ds_read_b128 v[220:223], v117 offset:2048
	ds_read_b128 v[224:227], v122 offset:4096
	ds_read_b128 v[228:231], v117 offset:4096
	ds_read_b128 v[232:235], v122 offset:6144
	ds_read_b128 v[236:239], v117 offset:6144
	ds_read_b64_tr_b16 v[130:131], v186 offset:0
	ds_read_b64_tr_b16 v[132:133], v186 offset:2048
	ds_read_b64_tr_b16 v[134:135], v188 offset:0
	ds_read_b64_tr_b16 v[136:137], v188 offset:2048
	ds_read_b64_tr_b16 v[138:139], v189 offset:0
	ds_read_b64_tr_b16 v[140:141], v189 offset:2048
	ds_read_b64_tr_b16 v[142:143], v190 offset:0
	ds_read_b64_tr_b16 v[144:145], v190 offset:2048

.Lmk_nomax:
	v_mov_b32_e32 v195, v201
	v_sub_f32_e32 v34, v34, v195
	v_fmamk_f32 v34, v34, 0x3fb8aa3b, v187
	v_exp_f32_e32 v34, v34
	s_nop 0
	v_cvt_f16_f32_e32 v34, v34
	v_cndmask_b32_e64 v34, 0, v34, s[56:57]
	ds_write_b16 v115, v34
	ds_read_b64_tr_b16 v[200:201], v193 offset:0
	ds_read_b64_tr_b16 v[202:203], v193 offset:512
	ds_read_b64_tr_b16 v[160:161], v193 offset:1024
	ds_read_b64_tr_b16 v[162:163], v193 offset:1536
	s_and_b64 vcc, exec, s[54:55]
	s_cbranch_vccnz .Lmk_first_path
	s_waitcnt vmcnt(0)
	s_waitcnt lgkmcnt(0)
	v_mfma_f32_16x16x32_f16 v[54:57], v[130:133], v[200:203], v[54:57]
	ds_write_b16 v115, v35
	ds_write_b128 v196, v[10:13]
	v_mfma_f32_16x16x32_f16 v[58:61], v[134:137], v[200:203], v[58:61]
	ds_write_b128 v196, v[14:17] offset:1024
	v_mfma_f32_16x16x32_f16 v[62:65], v[138:141], v[200:203], v[62:65]
	ds_write_b128 v196, v[30:33] offset:2048
	v_mfma_f32_16x16x32_f16 v[66:69], v[142:145], v[200:203], v[66:69]
	ds_write_b128 v196, v[26:29] offset:3072
	v_mfma_f32_16x16x32_f16 v[70:73], v[168:171], v[200:203], v[70:73]

.Lmk_st_done:
	s_cmp_lt_i32 s66, 33
	s_cbranch_scc1 .LBB2_76
	v_mfma_f32_16x16x32_f16 v[54:57], v[146:149], v[160:163], v[54:57]
	v_mfma_f32_16x16x32_f16 v[58:61], v[150:153], v[160:163], v[58:61]
	v_mfma_f32_16x16x32_f16 v[62:65], v[154:157], v[160:163], v[62:65]
	v_mfma_f32_16x16x32_f16 v[66:69], v[204:207], v[160:163], v[66:69]
	v_mfma_f32_16x16x32_f16 v[70:73], v[168:171], v[160:163], v[70:73]
.LBB2_76:
	s_and_b64 vcc, exec, s[54:55]
	s_cbranch_vccz .LBB2_110
	s_cmp_gt_i32 s50, 35
	s_cbranch_scc1 .LBB2_110
	s_add_i32 s36, s50, 2
	s_mul_hi_i32 s0, s36, 0x55555556
	s_lshr_b32 s1, s0, 31
	s_add_i32 s0, s0, s1
	s_mul_i32 s0, s0, 3
	s_sub_i32 s37, s36, s0
	s_mulk_i32 s37, 0xc00
	s_add_i32 s38, s40, s37
	v_lshl_add_u32 v36, v114, 2, v129
	s_and_saveexec_b64 s[0:1], s[4:5]
	v_lshl_add_u32 v37, v110, 2, s38
	ds_write_b32 v37, v194
	s_or_b64 exec, exec, s[0:1]
	v_lshl_add_u32 v37, v36, 2, s38
	v_lshlrev_b32_e32 v36, 2, v114
	v_sub_u32_e32 v36, v125, v36
	s_waitcnt vmcnt(8)
	v_cmp_lt_i32_e32 vcc, 0, v36
	s_and_saveexec_b64 s[0:1], vcc
	ds_write_b32 v37, v164 offset:64
	s_or_b64 exec, exec, s[0:1]
	v_cmp_lt_i32_e32 vcc, 1, v36
	s_and_saveexec_b64 s[0:1], vcc
	ds_write_b32 v37, v165 offset:68
	s_or_b64 exec, exec, s[0:1]
	v_cmp_lt_i32_e32 vcc, 2, v36
	s_and_saveexec_b64 s[0:1], vcc
	ds_write_b32 v37, v166 offset:72
	s_or_b64 exec, exec, s[0:1]
	v_cmp_lt_i32_e32 vcc, 3, v36
	s_and_saveexec_b64 s[0:1], vcc
	ds_write_b32 v37, v167 offset:76
	s_or_b64 exec, exec, s[0:1]
	v_add_u32_e32 v36, v129, v114
	v_cmp_lt_i32_e32 vcc, v119, v125
	s_and_saveexec_b64 s[0:1], vcc
	s_cbranch_execz .LBB2_109
	s_add_i32 s37, s47, s37
	v_lshl_add_u32 v130, v36, 2, s37
	v_lshlrev_b32_e32 v36, 2, v120
	v_mov_b32_e32 v37, 0
	v_mad_i64_i32 v[36:37], s[36:37], s36, v116, v[36:37]
	v_lshl_add_u64 v[36:37], v[0:1], 0, v[36:37]
	s_mov_b64 s[36:37], 0
	v_mov_b32_e32 v34, v119
	s_branch .LBB2_91
.LBB2_90:
	s_or_b64 exec, exec, s[38:39]
	v_add_u32_e32 v34, 4, v34
	v_cmp_ge_i32_e32 vcc, v34, v125
	v_add_u32_e32 v130, 16, v130
	s_or_b64 s[36:37], vcc, s[36:37]
	v_lshl_add_u64 v[36:37], v[36:37], 0, 16
	s_andn2_b64 exec, exec, s[36:37]
	s_cbranch_execz .LBB2_109

.Lmk_max:
	v_cndmask_b32_e64 v161, v185, v34, s[56:57]
	s_nop 1
	v_max_f32_dpp v161, v161, v161 row_shr:1 row_mask:0xf bank_mask:0xf
	v_mov_b32_e32 v121, v183
	s_nop 0
	v_max_f32_dpp v161, v161, v161 row_shr:2 row_mask:0xf bank_mask:0xf
	v_add_u32_e32 v229, s82, v172
	v_add_u32_e32 v230, s82, v173
	v_max_f32_dpp v161, v161, v161 row_shr:4 row_mask:0xf bank_mask:0xf
	ds_read_u16 v224, v229 offset:0
	ds_read_u16 v225, v229 offset:32
	v_max_f32_dpp v161, v161, v161 row_shr:8 row_mask:0xf bank_mask:0xf
	ds_read_u16 v226, v229 offset:64
	ds_read_u16 v227, v229 offset:96
	v_max_f32_dpp v161, v161, v161 row_bcast:15 row_mask:0xa bank_mask:0xf
	ds_read_u16 v232, v229 offset:128
	ds_read_u16 v233, v229 offset:160
	v_max_f32_dpp v161, v161, v161 row_bcast:31 row_mask:0xc bank_mask:0xf
	ds_read_u16 v234, v229 offset:192
	ds_read_u16 v235, v229 offset:224
	v_readlane_b32 s70, v161, 63
	ds_read_b32 v183, v230
	s_and_b64 vcc, exec, s[54:55]
	s_nop 0
	v_mov_b32_e32 v161, s70
	s_cbranch_vccz .Lmk_rescale

.Lmk_first_path:
	s_waitcnt vmcnt(8)
	s_waitcnt lgkmcnt(0)
	v_mfma_f32_16x16x32_f16 v[54:57], v[130:133], v[200:203], 0
	ds_write_b16 v115, v35
	ds_write_b128 v196, v[10:13]
	v_mfma_f32_16x16x32_f16 v[58:61], v[134:137], v[200:203], 0
	ds_write_b128 v196, v[14:17] offset:1024
	v_mfma_f32_16x16x32_f16 v[62:65], v[138:141], v[200:203], 0
	ds_write_b128 v196, v[30:33] offset:2048
	v_mfma_f32_16x16x32_f16 v[66:69], v[142:145], v[200:203], 0
	ds_write_b128 v196, v[26:29] offset:3072
	v_mfma_f32_16x16x32_f16 v[70:73], v[168:171], v[200:203], 0
	s_branch .Lmk_agg_join

.LBB2_93:
	s_lshl_b32 s0, s50, 7
	s_add_i32 s0, s0, 0x26000
	v_lshl_add_u32 v36, v107, 4, s0
	ds_read_b128 v[240:243], v36
	ds_read_b128 v[244:247], v36 offset:64
	s_cmp_gt_i32 s50, 35
	v_mov_b32_e32 v125, 0
	s_cbranch_scc1 .LBB2_103
	v_sub_u32_e32 v125, v174, v124
	s_add_i32 s0, s50, 2
	v_mov_b32_e32 v74, 0
	v_cndmask_b32_e64 v34, 0, v125, s[2:3]
	s_mul_i32 s0, s0, 0xc3500
	v_lshl_add_u32 v36, v124, 2, v118
	v_add_u32_dpp v34, v34, v34 row_shr:1 row_mask:0xf bank_mask:0xf bound_ctrl:1
	s_add_u32 s0, s90, s0
	s_addc_u32 s1, s91, 0
	v_add_u32_dpp v34, v34, v34 row_shr:2 row_mask:0xf bank_mask:0xf bound_ctrl:1
	v_mov_b32_e32 v120, v124
	s_nop 0
	v_add_u32_dpp v34, v34, v34 row_shr:4 row_mask:0xf bank_mask:0xf bound_ctrl:1
	global_load_dwordx4 v[164:167], v36, s[0:1]
	s_nop 0
	v_add_u32_dpp v34, v34, v34 row_shr:8 row_mask:0xf bank_mask:0xf bound_ctrl:1
	s_nop 1
	v_add_u32_dpp v34, v34, v34 row_bcast:15 row_mask:0xa bank_mask:0xf
	s_nop 1
	v_mov_b32_dpp v74, v34 row_bcast:31 row_mask:0xc bank_mask:0xf
	v_sub_u32_e32 v36, v74, v125
	v_add_u32_e32 v129, v36, v34
	v_sub_u32_e32 v36, 0x2f0, v129
	v_min_i32_e32 v125, v125, v36

	.amdhsa_kernel _Z6mainK2PKDF16_S0_S0_PKfPKiS4_S2_PfS0_S4_S4_
		.amdhsa_group_segment_fixed_size 160768
		.amdhsa_private_segment_fixed_size 0
		.amdhsa_kernarg_size 88
		.amdhsa_user_sgpr_count 2
		.amdhsa_user_sgpr_dispatch_ptr 0
		.amdhsa_user_sgpr_queue_ptr 0
		.amdhsa_user_sgpr_kernarg_segment_ptr 1
		.amdhsa_user_sgpr_dispatch_id 0
		.amdhsa_user_sgpr_kernarg_preload_length 0
		.amdhsa_user_sgpr_kernarg_preload_offset 0
		.amdhsa_user_sgpr_private_segment_size 0
		.amdhsa_uses_dynamic_stack 0
		.amdhsa_enable_private_segment 0
		.amdhsa_system_sgpr_workgroup_id_x 1
		.amdhsa_system_sgpr_workgroup_id_y 0
		.amdhsa_system_sgpr_workgroup_id_z 0
		.amdhsa_system_sgpr_workgroup_info 0
		.amdhsa_system_vgpr_workitem_id 0
		.amdhsa_next_free_vgpr 256
		.amdhsa_next_free_sgpr 96
		.amdhsa_accum_offset 256
		.amdhsa_reserve_vcc 1
		.amdhsa_float_round_mode_32 0
		.amdhsa_float_round_mode_16_64 0
		.amdhsa_float_denorm_mode_32 3
		.amdhsa_float_denorm_mode_16_64 3
		.amdhsa_dx10_clamp 1
		.amdhsa_ieee_mode 1
		.amdhsa_fp16_overflow 0
		.amdhsa_tg_split 0
		.amdhsa_exception_fp_ieee_invalid_op 0
		.amdhsa_exception_fp_denorm_src 0
		.amdhsa_exception_fp_ieee_div_zero 0
		.amdhsa_exception_fp_ieee_overflow 0
		.amdhsa_exception_fp_ieee_underflow 0
		.amdhsa_exception_fp_ieee_inexact 0
		.amdhsa_exception_int_div_zero 0
	.end_amdhsa_kernel

amdhsa.kernels:
  - .agpr_count:     0
    .args:
      - .actual_access:  read_only
        .address_space:  global
        .offset:         0
        .size:           8
        .value_kind:     global_buffer
      - .actual_access:  write_only
        .address_space:  global
        .offset:         8
        .size:           8
        .value_kind:     global_buffer
      - .actual_access:  write_only
        .address_space:  global
        .offset:         16
        .size:           8
        .value_kind:     global_buffer
      - .actual_access:  read_only
        .address_space:  global
        .offset:         24
        .size:           8
        .value_kind:     global_buffer
      - .actual_access:  read_only
        .address_space:  global
        .offset:         32
        .size:           8
        .value_kind:     global_buffer
      - .actual_access:  read_only
        .address_space:  global
        .offset:         40
        .size:           8
        .value_kind:     global_buffer
      - .actual_access:  read_only
        .address_space:  global
        .offset:         48
        .size:           8
        .value_kind:     global_buffer
      - .actual_access:  read_only
        .address_space:  global
        .offset:         56
        .size:           8
        .value_kind:     global_buffer
      - .actual_access:  read_only
        .address_space:  global
        .offset:         64
        .size:           8
        .value_kind:     global_buffer
      - .actual_access:  write_only
        .address_space:  global
        .offset:         72
        .size:           8
        .value_kind:     global_buffer
      - .actual_access:  write_only
        .address_space:  global
        .offset:         80
        .size:           8
        .value_kind:     global_buffer
      - .actual_access:  write_only
        .address_space:  global
        .offset:         88
        .size:           8
        .value_kind:     global_buffer
      - .actual_access:  write_only
        .address_space:  global
        .offset:         96
        .size:           8
        .value_kind:     global_buffer
      - .actual_access:  write_only
        .address_space:  global
        .offset:         104
        .size:           8
        .value_kind:     global_buffer
      - .actual_access:  read_only
        .address_space:  global
        .offset:         112
        .size:           8
        .value_kind:     global_buffer
      - .actual_access:  write_only
        .address_space:  global
        .offset:         120
        .size:           8
        .value_kind:     global_buffer
      - .actual_access:  write_only
        .address_space:  global
        .offset:         128
        .size:           8
        .value_kind:     global_buffer
    .group_segment_fixed_size: 58224
    .kernarg_segment_align: 8
    .kernarg_segment_size: 136
    .language:       OpenCL C
    .language_version:
      - 2
      - 0
    .max_flat_workgroup_size: 512
    .name:           _Z6fusedKPKiPiS1_PKfS3_S3_S3_S3_S3_PDF16_PfS5_S4_S5_S3_S4_S1_
    .private_segment_fixed_size: 0
    .sgpr_count:     44
    .sgpr_spill_count: 0
    .symbol:         _Z6fusedKPKiPiS1_PKfS3_S3_S3_S3_S3_PDF16_PfS5_S4_S5_S3_S4_S1_.kd
    .uniform_work_group_size: 1
    .uses_dynamic_stack: false
    .vgpr_count:     126
    .vgpr_spill_count: 0
    .wavefront_size: 64
  - .agpr_count:     16
    .args:
      - .actual_access:  read_only
        .address_space:  global
        .offset:         0
        .size:           8
        .value_kind:     global_buffer
      - .actual_access:  read_only
        .address_space:  global
        .offset:         8
        .size:           8
        .value_kind:     global_buffer
      - .actual_access:  write_only
        .address_space:  global
        .offset:         16
        .size:           8
        .value_kind:     global_buffer
      - .actual_access:  read_only
        .address_space:  global
        .offset:         24
        .size:           8
        .value_kind:     global_buffer
      - .actual_access:  read_only
        .address_space:  global
        .offset:         32
        .size:           8
        .value_kind:     global_buffer
      - .actual_access:  write_only
        .address_space:  global
        .offset:         40
        .size:           8
        .value_kind:     global_buffer
      - .actual_access:  read_only
        .address_space:  global
        .offset:         48
        .size:           8
        .value_kind:     global_buffer
      - .offset:         56
        .size:           4
        .value_kind:     by_value
      - .address_space:  global
        .offset:         64
        .size:           8
        .value_kind:     global_buffer
      - .actual_access:  write_only
        .address_space:  global
        .offset:         72
        .size:           8
        .value_kind:     global_buffer
      - .offset:         80
        .size:           4
        .value_kind:     hidden_block_count_x
      - .offset:         84
        .size:           4
        .value_kind:     hidden_block_count_y
      - .offset:         88
        .size:           4
        .value_kind:     hidden_block_count_z
      - .offset:         92
        .size:           2
        .value_kind:     hidden_group_size_x
      - .offset:         94
        .size:           2
        .value_kind:     hidden_group_size_y
      - .offset:         96
        .size:           2
        .value_kind:     hidden_group_size_z
      - .offset:         98
        .size:           2
        .value_kind:     hidden_remainder_x
      - .offset:         100
        .size:           2
        .value_kind:     hidden_remainder_y
      - .offset:         102
        .size:           2
        .value_kind:     hidden_remainder_z
      - .offset:         120
        .size:           8
        .value_kind:     hidden_global_offset_x
      - .offset:         128
        .size:           8
        .value_kind:     hidden_global_offset_y
      - .offset:         136
        .size:           8
        .value_kind:     hidden_global_offset_z
      - .offset:         144
        .size:           2
        .value_kind:     hidden_grid_dims
    .group_segment_fixed_size: 0
    .kernarg_segment_align: 8
    .kernarg_segment_size: 336
    .language:       OpenCL C
    .language_version:
      - 2
      - 0
    .max_flat_workgroup_size: 256
    .name:           _Z5stabKPKfS0_PfPKDF16_S3_PDF16_PKiiPiS7_
    .private_segment_fixed_size: 0
    .sgpr_count:     34
    .sgpr_spill_count: 0
    .symbol:         _Z5stabKPKfS0_PfPKDF16_S3_PDF16_PKiiPiS7_.kd
    .uniform_work_group_size: 1
    .uses_dynamic_stack: false
    .vgpr_count:     68
    .vgpr_spill_count: 0
    .wavefront_size: 64
  - .agpr_count:     0
    .args:
      - .actual_access:  read_only
        .address_space:  global
        .offset:         0
        .size:           8
        .value_kind:     global_buffer
      - .actual_access:  read_only
        .address_space:  global
        .offset:         8
        .size:           8
        .value_kind:     global_buffer
      - .actual_access:  read_only
        .address_space:  global
        .offset:         16
        .size:           8
        .value_kind:     global_buffer
      - .actual_access:  read_only
        .address_space:  global
        .offset:         24
        .size:           8
        .value_kind:     global_buffer
      - .actual_access:  read_only
        .address_space:  global
        .offset:         32
        .size:           8
        .value_kind:     global_buffer
      - .actual_access:  read_only
        .address_space:  global
        .offset:         40
        .size:           8
        .value_kind:     global_buffer
      - .actual_access:  read_only
        .address_space:  global
        .offset:         48
        .size:           8
        .value_kind:     global_buffer
      - .actual_access:  write_only
        .address_space:  global
        .offset:         56
        .size:           8
        .value_kind:     global_buffer
      - .actual_access:  read_only
        .address_space:  global
        .offset:         64
        .size:           8
        .value_kind:     global_buffer
      - .actual_access:  read_only
        .address_space:  global
        .offset:         72
        .size:           8
        .value_kind:     global_buffer
      - .actual_access:  read_only
        .address_space:  global
        .offset:         80
        .size:           8
        .value_kind:     global_buffer
    .group_segment_fixed_size: 160768
    .kernarg_segment_align: 8
    .kernarg_segment_size: 88
    .language:       OpenCL C
    .language_version:
      - 2
      - 0
    .max_flat_workgroup_size: 512
    .name:           _Z6mainK2PKDF16_S0_S0_PKfPKiS4_S2_PfS0_S4_S4_
    .private_segment_fixed_size: 0
    .sgpr_count:     60
    .sgpr_spill_count: 0
    .symbol:         _Z6mainK2PKDF16_S0_S0_PKfPKiS4_S2_PfS0_S4_S4_.kd
    .uniform_work_group_size: 1
    .uses_dynamic_stack: false
    .vgpr_count:     256
    .vgpr_spill_count: 0
    .wavefront_size: 64
